# top-k hosted conversion units staggered by wave as well
# baseline (speedup 1.0000x reference)
; #define LAS __attribute__((address_space(3)))
; __device__ __forceinline__ void router_topk(Frame& F, int tile) {
;     const float* logits = WSP(F, WS_B, float); const float* br = F.a->in[I_BR];
;     int* tk_e = WSP(F, WS_TOPK_E, int); float* tk_g = WSP(F, WS_TOPK_G, float); int* tk_p = WSP(F, WS_TOPK_P, int);
;     int* gcnt = (int*)(F.a->ws + WS_CTL + CTL_CNT);
;     LAS int* hist = (LAS int*)F.lds; LAS int* base = hist + 256;
;     const int lane = F.lane, w = F.wave;
;     if (F.tid < 256) hist[F.tid] = 0;
;     __syncthreads();
;     const f32x4 bias = *(const f32x4*)(br + 4 * lane);
;     f32x4 lgn = *(const f32x4*)(logits + (size_t)(tile * 256 + w * 32) * 256 + 4 * lane);
;     int pe = 0, pp = 0; float pg = 0.f;
;     int* dumpi = (int*)(F.a->ws + WS_B + ((size_t)128 << 20));
.Lcvt_vcu:
	s_add_u32 s69, s41, s40
	s_and_b32 s69, s69, 3
	s_lshl_b32 s41, s41, 3
	s_add_u32 s89, s41, s40
	s_lshl_b32 s71, s64, 3
	s_mul_i32 s39, s71, 12
	s_add_u32 s89, s89, s39
	s_movk_i32 s90, 8
	s_mov_b32 s32, 0
	s_add_u32 s86, s84, 0x9180000
	s_addc_u32 s87, s85, 0
	s_add_u32 s84, s84, 0x1100000
	s_addc_u32 s85, s85, 0
	s_add_u32 s14, s8, 0x900000
	s_addc_u32 s15, s9, 0
	s_add_u32 s16, s8, 0xb00000
	s_addc_u32 s17, s9, 0
	s_add_u32 s18, s8, 0xd00000
	s_addc_u32 s19, s9, 0
	v_mov_b32_e32 v131, 0
	s_add_u32 s20, s8, 0x4000
	v_mov_b32_e32 v133, v131
	s_addc_u32 s21, s9, 0
	v_lshl_add_u64 v[2:3], s[8:9], 0, v[132:133]
	s_mov_b64 s[8:9], 0x1d1c0000
	s_waitcnt vmcnt(0)
	v_lshl_add_u64 v[12:13], v[2:3], 0, s[8:9]
	s_mov_b64 s[8:9], 0x1d1c0100
	s_movk_i32 s4, 0x100
	v_mov_b32_e32 v135, v131
	v_lshl_add_u64 v[14:15], v[2:3], 0, s[8:9]
	s_mov_b64 s[8:9], 0x1d1c0200
	v_cmp_gt_i32_e64 s[4:5], s4, v1
	s_mov_b32 s26, 0
	v_lshl_add_u32 v22, v1, 2, 0
	s_lshl_b32 s27, s49, 5
	v_lshl_add_u64 v[10:11], s[6:7], 0, v[134:135]
	v_cmp_gt_u32_e64 s[6:7], 8, v130
	v_lshl_add_u64 v[16:17], v[2:3], 0, s[8:9]
	v_mov_b64_e32 v[18:19], 0x100
	v_mov_b64_e32 v[20:21], 0xff
	v_mov_b32_e32 v23, 0xff800000
	v_mov_b32_e32 v24, 1
	s_waitcnt vmcnt(0)
	s_barrier
	s_branch .LBB0_532
